# v45 + e2f computed in the scan phase (which has slack) instead of after the gather
# speedup vs baseline: 1.0123x; 1.0123x over previous
_Z7vq_mainPKfPKiS0_PfPhPdPi:
	s_load_dwordx4 s[4:7], s[0:1], 0x0
	s_load_dwordx2 s[22:23], s[0:1], 0x10
	s_load_dwordx2 s[20:21], s[0:1], 0x18
	s_load_dwordx4 s[12:15], s[0:1], 0x20
	s_load_dwordx2 s[10:11], s[0:1], 0x30
	s_and_b32 s3, s2, 7
	s_lshl_b32 s3, s3, 6
	s_lshr_b32 s16, s2, 3
	s_add_i32 s16, s16, s3
	s_lshr_b32 s18, s16, 5
	s_mov_b32 s19, 0
	s_and_b32 s28, s16, 31
	s_lshl_b32 s28, s28, 4
	s_add_i32 s29, s28, 1
	v_readfirstlane_b32 s17, v0
	v_and_b32_e32 v1, 63, v0
	v_lshlrev_b32_e32 v66, 4, v0
	s_lshr_b32 s17, s17, 6
	s_lshl_b32 s24, s17, 4
	s_lshl_b32 s30, s18, 15
	s_lshl_b32 s31, s18, 23
	v_add_u32_e32 v67, 0x1000, v66
	v_add_u32_e32 v68, 0x2000, v66
	v_add_u32_e32 v69, 0x3000, v66
	v_add_u32_e32 v70, 0x4000, v66
	v_add_u32_e32 v71, 0x5000, v66
	v_add_u32_e32 v72, 0x6000, v66
	v_add_u32_e32 v73, 0x7000, v66
	s_movk_i32 s9, 0x810
	s_mov_b32 s3, 0x8100
	s_mul_i32 s36, s29, 0x810
	v_mov_b32_e32 v141, s36
	v_sub_u32_e32 v141, 0, v141
	s_waitcnt lgkmcnt(0)
	s_add_u32 s34, s6, s30
	s_addc_u32 s35, s7, 0
	s_add_u32 s32, s4, s31
	s_addc_u32 s33, s5, 0
	global_load_dwordx4 v[74:77], v66, s[34:35]
	global_load_dwordx4 v[78:81], v67, s[34:35]
	global_load_dwordx4 v[82:85], v68, s[34:35]
	global_load_dwordx4 v[86:89], v69, s[34:35]
	global_load_dwordx4 v[90:93], v70, s[34:35]
	global_load_dwordx4 v[94:97], v71, s[34:35]
	global_load_dwordx4 v[98:101], v72, s[34:35]
	global_load_dwordx4 v[102:105], v73, s[34:35]
	v_and_b32_e32 v150, 15, v0
	v_or_b32_e32 v150, s24, v150
	v_and_b32_e32 v151, 48, v0
	v_lshl_or_b32 v150, v150, 10, v151
	global_load_dwordx4 v[62:65], v150, s[22:23] offset:0
	global_load_dwordx4 v[58:61], v150, s[22:23] offset:64
	global_load_dwordx4 v[54:57], v150, s[22:23] offset:128
	global_load_dwordx4 v[50:53], v150, s[22:23] offset:192
	global_load_dwordx4 v[46:49], v150, s[22:23] offset:256
	global_load_dwordx4 v[42:45], v150, s[22:23] offset:320
	global_load_dwordx4 v[38:41], v150, s[22:23] offset:384
	global_load_dwordx4 v[34:37], v150, s[22:23] offset:448
	global_load_dwordx4 v[30:33], v150, s[22:23] offset:512
	global_load_dwordx4 v[26:29], v150, s[22:23] offset:576
	global_load_dwordx4 v[22:25], v150, s[22:23] offset:640
	global_load_dwordx4 v[18:21], v150, s[22:23] offset:704
	global_load_dwordx4 v[14:17], v150, s[22:23] offset:768
	global_load_dwordx4 v[10:13], v150, s[22:23] offset:832
	global_load_dwordx4 v[6:9], v150, s[22:23] offset:896
	global_load_dwordx4 v[2:5], v150, s[22:23] offset:960
	v_mov_b32_e32 v142, 1
	v_mov_b32_e32 v143, 4
	v_mov_b32_e32 v144, 0x11100
	v_lshlrev_b32_e32 v145, 8, v0
	v_lshlrev_b32_e32 v148, 3, v0
	v_mov_b32_e32 v152, 0
	v_mov_b32_e32 v153, 0
	ds_write_b64 v148, v[152:153] offset:32768
	ds_write_b64 v148, v[152:153] offset:34832
	ds_write_b64 v148, v[152:153] offset:36896
	ds_write_b64 v148, v[152:153] offset:38960
	ds_write_b64 v148, v[152:153] offset:41024
	ds_write_b64 v148, v[152:153] offset:43088
	ds_write_b64 v148, v[152:153] offset:45152
	ds_write_b64 v148, v[152:153] offset:47216
	ds_write_b64 v148, v[152:153] offset:49280
	ds_write_b64 v148, v[152:153] offset:51344
	ds_write_b64 v148, v[152:153] offset:53408
	ds_write_b64 v148, v[152:153] offset:55472
	ds_write_b64 v148, v[152:153] offset:57536
	ds_write_b64 v148, v[152:153] offset:59600
	ds_write_b64 v148, v[152:153] offset:61664
	ds_write_b64 v148, v[152:153] offset:63728
	v_cmp_gt_u32_e32 vcc, 16, v0
	s_and_saveexec_b64 s[30:31], vcc
	v_mul_u32_u24_e32 v151, 0x810, v0
	ds_write_b64 v151, v[152:153] offset:34816
	v_mov_b32_e32 v150, 0x11540
	v_mov_b32_e32 v149, 8
	ds_write_b32 v150, v149
	s_mov_b64 exec, s[30:31]
	s_waitcnt lgkmcnt(0)
	s_barrier
	s_waitcnt vmcnt(16)
	v_mad_u32_u24 v74, v74, s9, v141
	v_mad_u32_u24 v75, v75, s9, v141
	v_mad_u32_u24 v76, v76, s9, v141
	v_mad_u32_u24 v77, v77, s9, v141
	v_mad_u32_u24 v78, v78, s9, v141
	v_mad_u32_u24 v79, v79, s9, v141
	v_mad_u32_u24 v80, v80, s9, v141
	v_mad_u32_u24 v81, v81, s9, v141
	v_mad_u32_u24 v82, v82, s9, v141
	v_mad_u32_u24 v83, v83, s9, v141
	v_mad_u32_u24 v84, v84, s9, v141
	v_mad_u32_u24 v85, v85, s9, v141
	v_mad_u32_u24 v86, v86, s9, v141
	v_mad_u32_u24 v87, v87, s9, v141
	v_mad_u32_u24 v88, v88, s9, v141
	v_mad_u32_u24 v89, v89, s9, v141
	v_mad_u32_u24 v90, v90, s9, v141
	v_mad_u32_u24 v91, v91, s9, v141
	v_mad_u32_u24 v92, v92, s9, v141
	v_mad_u32_u24 v93, v93, s9, v141
	v_mad_u32_u24 v94, v94, s9, v141
	v_mad_u32_u24 v95, v95, s9, v141
	v_mad_u32_u24 v96, v96, s9, v141
	v_mad_u32_u24 v97, v97, s9, v141
	v_mad_u32_u24 v98, v98, s9, v141
	v_mad_u32_u24 v99, v99, s9, v141
	v_mad_u32_u24 v100, v100, s9, v141
	v_mad_u32_u24 v101, v101, s9, v141
	v_mad_u32_u24 v102, v102, s9, v141
	v_mad_u32_u24 v103, v103, s9, v141
	v_mad_u32_u24 v104, v104, s9, v141
	v_mad_u32_u24 v105, v105, s9, v141
	v_cmp_gt_u32_e64 s[36:37], s3, v74
	v_cmp_gt_u32_e64 s[38:39], s3, v75
	v_cmp_gt_u32_e64 s[40:41], s3, v76
	v_cmp_gt_u32_e64 s[42:43], s3, v77
	v_cmp_gt_u32_e64 s[44:45], s3, v78
	v_cmp_gt_u32_e64 s[46:47], s3, v79
	v_cmp_gt_u32_e64 s[48:49], s3, v80
	v_cmp_gt_u32_e64 s[50:51], s3, v81
	v_cmp_gt_u32_e64 s[52:53], s3, v82
	v_cmp_gt_u32_e64 s[54:55], s3, v83
	v_cmp_gt_u32_e64 s[56:57], s3, v84
	v_cmp_gt_u32_e64 s[58:59], s3, v85
	v_cmp_gt_u32_e64 s[60:61], s3, v86
	v_cmp_gt_u32_e64 s[62:63], s3, v87
	v_cmp_gt_u32_e64 s[64:65], s3, v88
	v_cmp_gt_u32_e64 s[66:67], s3, v89
	v_cmp_gt_u32_e64 s[68:69], s3, v90
	v_cmp_gt_u32_e64 s[70:71], s3, v91
	v_cmp_gt_u32_e64 s[72:73], s3, v92
	v_cmp_gt_u32_e64 s[74:75], s3, v93
	v_cmp_gt_u32_e64 s[76:77], s3, v94
	v_cmp_gt_u32_e64 s[78:79], s3, v95
	v_cmp_gt_u32_e64 s[80:81], s3, v96
	v_cmp_gt_u32_e64 s[82:83], s3, v97
	v_cmp_gt_u32_e64 s[84:85], s3, v98
	v_cmp_gt_u32_e64 s[86:87], s3, v99
	v_cmp_gt_u32_e64 s[88:89], s3, v100
	v_cmp_gt_u32_e64 s[90:91], s3, v101
	v_cmp_gt_u32_e64 s[92:93], s3, v102
	v_cmp_gt_u32_e64 s[94:95], s3, v103
	v_cmp_gt_u32_e64 s[96:97], s3, v104
	v_cmp_gt_u32_e64 s[98:99], s3, v105
	s_mov_b64 exec, s[36:37]
	ds_add_u32 v74, v142 offset:34816
	s_mov_b64 exec, s[38:39]
	ds_add_u32 v75, v142 offset:34816
	s_mov_b64 exec, s[40:41]
	ds_add_u32 v76, v142 offset:34816
	s_mov_b64 exec, s[42:43]
	ds_add_u32 v77, v142 offset:34816
	s_mov_b64 exec, s[44:45]
	ds_add_u32 v78, v142 offset:34816
	s_mov_b64 exec, s[46:47]
	ds_add_u32 v79, v142 offset:34816
	s_mov_b64 exec, s[48:49]
	ds_add_u32 v80, v142 offset:34816
	s_mov_b64 exec, s[50:51]
	ds_add_u32 v81, v142 offset:34816
	s_mov_b64 exec, s[52:53]
	ds_add_u32 v82, v142 offset:34816
	s_mov_b64 exec, s[54:55]
	ds_add_u32 v83, v142 offset:34816
	s_mov_b64 exec, s[56:57]
	ds_add_u32 v84, v142 offset:34816
	s_mov_b64 exec, s[58:59]
	ds_add_u32 v85, v142 offset:34816
	s_mov_b64 exec, s[60:61]
	ds_add_u32 v86, v142 offset:34816
	s_mov_b64 exec, s[62:63]
	ds_add_u32 v87, v142 offset:34816
	s_mov_b64 exec, s[64:65]
	ds_add_u32 v88, v142 offset:34816
	s_mov_b64 exec, s[66:67]
	ds_add_u32 v89, v142 offset:34816
	s_mov_b64 exec, s[68:69]
	ds_add_u32 v90, v142 offset:34816
	s_mov_b64 exec, s[70:71]
	ds_add_u32 v91, v142 offset:34816
	s_mov_b64 exec, s[72:73]
	ds_add_u32 v92, v142 offset:34816
	s_mov_b64 exec, s[74:75]
	ds_add_u32 v93, v142 offset:34816
	s_mov_b64 exec, s[76:77]
	ds_add_u32 v94, v142 offset:34816
	s_mov_b64 exec, s[78:79]
	ds_add_u32 v95, v142 offset:34816
	s_mov_b64 exec, s[80:81]
	ds_add_u32 v96, v142 offset:34816
	s_mov_b64 exec, s[82:83]
	ds_add_u32 v97, v142 offset:34816
	s_mov_b64 exec, s[84:85]
	ds_add_u32 v98, v142 offset:34816
	s_mov_b64 exec, s[86:87]
	ds_add_u32 v99, v142 offset:34816
	s_mov_b64 exec, s[88:89]
	ds_add_u32 v100, v142 offset:34816
	s_mov_b64 exec, s[90:91]
	ds_add_u32 v101, v142 offset:34816
	s_mov_b64 exec, s[92:93]
	ds_add_u32 v102, v142 offset:34816
	s_mov_b64 exec, s[94:95]
	ds_add_u32 v103, v142 offset:34816
	s_mov_b64 exec, s[96:97]
	ds_add_u32 v104, v142 offset:34816
	s_mov_b64 exec, s[98:99]
	ds_add_u32 v105, v142 offset:34816
	s_mov_b64 exec, -1
	s_waitcnt lgkmcnt(0)
	s_barrier
	v_and_b32_e32 v67, 15, v0
	v_mul_u32_u24_e32 v67, 0x810, v67
	ds_read_b32 v68, v67 offset:34816
	s_waitcnt lgkmcnt(0)
	v_mov_b32_e32 v69, v68
	s_nop 1
	v_add_u32_dpp v69, v69, v69 row_shr:1 row_mask:0xf bank_mask:0xf bound_ctrl:1
	s_nop 1
	v_add_u32_dpp v69, v69, v69 row_shr:2 row_mask:0xf bank_mask:0xf bound_ctrl:1
	s_nop 1
	v_add_u32_dpp v69, v69, v69 row_shr:4 row_mask:0xf bank_mask:0xf bound_ctrl:1
	s_nop 1
	v_add_u32_dpp v69, v69, v69 row_shr:8 row_mask:0xf bank_mask:0xf bound_ctrl:1
	s_nop 1
	v_sub_u32_e32 v70, v69, v68
	v_lshlrev_b32_e32 v70, 2, v70
	v_readlane_b32 s8, v69, 15
	s_cmp_lg_u32 s17, 0
	s_cbranch_scc1 .Lfront_nocursor
	v_cmp_gt_u32_e32 vcc, 16, v1
	s_and_saveexec_b64 s[30:31], vcc
	ds_write_b32 v67, v70 offset:34820
	s_mov_b64 exec, s[30:31]
.Lfront_nocursor:
	s_waitcnt lgkmcnt(0)
	s_barrier
	s_mov_b64 exec, s[36:37]
	ds_add_rtn_u32 v106, v74, v143 offset:34820
	s_mov_b64 exec, s[38:39]
	ds_add_rtn_u32 v107, v75, v143 offset:34820
	s_mov_b64 exec, s[40:41]
	ds_add_rtn_u32 v108, v76, v143 offset:34820
	s_mov_b64 exec, s[42:43]
	ds_add_rtn_u32 v109, v77, v143 offset:34820
	s_mov_b64 exec, s[44:45]
	ds_add_rtn_u32 v110, v78, v143 offset:34820
	s_mov_b64 exec, s[46:47]
	ds_add_rtn_u32 v111, v79, v143 offset:34820
	s_mov_b64 exec, s[48:49]
	ds_add_rtn_u32 v112, v80, v143 offset:34820
	s_mov_b64 exec, s[50:51]
	ds_add_rtn_u32 v113, v81, v143 offset:34820
	s_mov_b64 exec, s[52:53]
	ds_add_rtn_u32 v114, v82, v143 offset:34820
	s_mov_b64 exec, s[54:55]
	ds_add_rtn_u32 v115, v83, v143 offset:34820
	s_mov_b64 exec, s[56:57]
	ds_add_rtn_u32 v116, v84, v143 offset:34820
	s_mov_b64 exec, s[58:59]
	ds_add_rtn_u32 v117, v85, v143 offset:34820
	s_mov_b64 exec, s[60:61]
	ds_add_rtn_u32 v118, v86, v143 offset:34820
	s_mov_b64 exec, s[62:63]
	ds_add_rtn_u32 v119, v87, v143 offset:34820
	s_mov_b64 exec, s[64:65]
	ds_add_rtn_u32 v120, v88, v143 offset:34820
	s_mov_b64 exec, s[66:67]
	ds_add_rtn_u32 v121, v89, v143 offset:34820
	s_mov_b64 exec, s[68:69]
	ds_add_rtn_u32 v122, v90, v143 offset:34820
	s_mov_b64 exec, s[70:71]
	ds_add_rtn_u32 v123, v91, v143 offset:34820
	s_mov_b64 exec, s[72:73]
	ds_add_rtn_u32 v124, v92, v143 offset:34820
	s_mov_b64 exec, s[74:75]
	ds_add_rtn_u32 v125, v93, v143 offset:34820
	s_mov_b64 exec, s[76:77]
	ds_add_rtn_u32 v126, v94, v143 offset:34820
	s_mov_b64 exec, s[78:79]
	ds_add_rtn_u32 v127, v95, v143 offset:34820
	s_mov_b64 exec, s[80:81]
	ds_add_rtn_u32 v128, v96, v143 offset:34820
	s_mov_b64 exec, s[82:83]
	ds_add_rtn_u32 v129, v97, v143 offset:34820
	s_mov_b64 exec, s[84:85]
	ds_add_rtn_u32 v130, v98, v143 offset:34820
	s_mov_b64 exec, s[86:87]
	ds_add_rtn_u32 v131, v99, v143 offset:34820
	s_mov_b64 exec, s[88:89]
	ds_add_rtn_u32 v132, v100, v143 offset:34820
	s_mov_b64 exec, s[90:91]
	ds_add_rtn_u32 v133, v101, v143 offset:34820
	s_mov_b64 exec, s[92:93]
	ds_add_rtn_u32 v134, v102, v143 offset:34820
	s_mov_b64 exec, s[94:95]
	ds_add_rtn_u32 v135, v103, v143 offset:34820
	s_mov_b64 exec, s[96:97]
	ds_add_rtn_u32 v136, v104, v143 offset:34820
	s_mov_b64 exec, s[98:99]
	ds_add_rtn_u32 v137, v105, v143 offset:34820
	s_mov_b64 exec, -1
	v_lshlrev_b32_e32 v145, 18, v0
	v_add_u32_e32 v146, 0x0, v145
	v_or_b32_e32 v74, v146, v74
	v_add_u32_e32 v147, 0x10000, v145
	v_or_b32_e32 v75, v147, v75
	v_add_u32_e32 v146, 0x20000, v145
	v_or_b32_e32 v76, v146, v76
	v_add_u32_e32 v147, 0x30000, v145
	v_or_b32_e32 v77, v147, v77
	v_add_u32_e32 v146, 0x4000000, v145
	v_or_b32_e32 v78, v146, v78
	v_add_u32_e32 v147, 0x4010000, v145
	v_or_b32_e32 v79, v147, v79
	v_add_u32_e32 v146, 0x4020000, v145
	v_or_b32_e32 v80, v146, v80
	v_add_u32_e32 v147, 0x4030000, v145
	v_or_b32_e32 v81, v147, v81
	v_add_u32_e32 v146, 0x8000000, v145
	v_or_b32_e32 v82, v146, v82
	v_add_u32_e32 v147, 0x8010000, v145
	v_or_b32_e32 v83, v147, v83
	v_add_u32_e32 v146, 0x8020000, v145
	v_or_b32_e32 v84, v146, v84
	v_add_u32_e32 v147, 0x8030000, v145
	v_or_b32_e32 v85, v147, v85
	v_add_u32_e32 v146, 0xc000000, v145
	v_or_b32_e32 v86, v146, v86
	v_add_u32_e32 v147, 0xc010000, v145
	v_or_b32_e32 v87, v147, v87
	v_add_u32_e32 v146, 0xc020000, v145
	v_or_b32_e32 v88, v146, v88
	v_add_u32_e32 v147, 0xc030000, v145
	v_or_b32_e32 v89, v147, v89
	v_add_u32_e32 v146, 0x10000000, v145
	v_or_b32_e32 v90, v146, v90
	v_add_u32_e32 v147, 0x10010000, v145
	v_or_b32_e32 v91, v147, v91
	v_add_u32_e32 v146, 0x10020000, v145
	v_or_b32_e32 v92, v146, v92
	v_add_u32_e32 v147, 0x10030000, v145
	v_or_b32_e32 v93, v147, v93
	v_add_u32_e32 v146, 0x14000000, v145
	v_or_b32_e32 v94, v146, v94
	v_add_u32_e32 v147, 0x14010000, v145
	v_or_b32_e32 v95, v147, v95
	v_add_u32_e32 v146, 0x14020000, v145
	v_or_b32_e32 v96, v146, v96
	v_add_u32_e32 v147, 0x14030000, v145
	v_or_b32_e32 v97, v147, v97
	v_add_u32_e32 v146, 0x18000000, v145
	v_or_b32_e32 v98, v146, v98
	v_add_u32_e32 v147, 0x18010000, v145
	v_or_b32_e32 v99, v147, v99
	v_add_u32_e32 v146, 0x18020000, v145
	v_or_b32_e32 v100, v146, v100
	v_add_u32_e32 v147, 0x18030000, v145
	v_or_b32_e32 v101, v147, v101
	v_add_u32_e32 v146, 0x1c000000, v145
	v_or_b32_e32 v102, v146, v102
	v_add_u32_e32 v147, 0x1c010000, v145
	v_or_b32_e32 v103, v147, v103
	v_add_u32_e32 v146, 0x1c020000, v145
	v_or_b32_e32 v104, v146, v104
	v_add_u32_e32 v147, 0x1c030000, v145
	v_or_b32_e32 v105, v147, v105
	s_waitcnt lgkmcnt(0)
	s_mov_b64 exec, s[36:37]
	ds_write_b32 v106, v74
	s_mov_b64 exec, s[38:39]
	ds_write_b32 v107, v75
	s_mov_b64 exec, s[40:41]
	ds_write_b32 v108, v76
	s_mov_b64 exec, s[42:43]
	ds_write_b32 v109, v77
	s_mov_b64 exec, s[44:45]
	ds_write_b32 v110, v78
	s_mov_b64 exec, s[46:47]
	ds_write_b32 v111, v79
	s_mov_b64 exec, s[48:49]
	ds_write_b32 v112, v80
	s_mov_b64 exec, s[50:51]
	ds_write_b32 v113, v81
	s_mov_b64 exec, s[52:53]
	ds_write_b32 v114, v82
	s_mov_b64 exec, s[54:55]
	ds_write_b32 v115, v83
	s_mov_b64 exec, s[56:57]
	ds_write_b32 v116, v84
	s_mov_b64 exec, s[58:59]
	ds_write_b32 v117, v85
	s_mov_b64 exec, s[60:61]
	ds_write_b32 v118, v86
	s_mov_b64 exec, s[62:63]
	ds_write_b32 v119, v87
	s_mov_b64 exec, s[64:65]
	ds_write_b32 v120, v88
	s_mov_b64 exec, s[66:67]
	ds_write_b32 v121, v89
	s_mov_b64 exec, s[68:69]
	ds_write_b32 v122, v90
	s_mov_b64 exec, s[70:71]
	ds_write_b32 v123, v91
	s_mov_b64 exec, s[72:73]
	ds_write_b32 v124, v92
	s_mov_b64 exec, s[74:75]
	ds_write_b32 v125, v93
	s_mov_b64 exec, s[76:77]
	ds_write_b32 v126, v94
	s_mov_b64 exec, s[78:79]
	ds_write_b32 v127, v95
	s_mov_b64 exec, s[80:81]
	ds_write_b32 v128, v96
	s_mov_b64 exec, s[82:83]
	ds_write_b32 v129, v97
	s_mov_b64 exec, s[84:85]
	ds_write_b32 v130, v98
	s_mov_b64 exec, s[86:87]
	ds_write_b32 v131, v99
	s_mov_b64 exec, s[88:89]
	ds_write_b32 v132, v100
	s_mov_b64 exec, s[90:91]
	ds_write_b32 v133, v101
	s_mov_b64 exec, s[92:93]
	ds_write_b32 v134, v102
	s_mov_b64 exec, s[94:95]
	ds_write_b32 v135, v103
	s_mov_b64 exec, s[96:97]
	ds_write_b32 v136, v104
	s_mov_b64 exec, s[98:99]
	ds_write_b32 v137, v105
	s_mov_b64 exec, -1
	s_waitcnt lgkmcnt(0)
	s_barrier
	v_lshlrev_b32_e32 v218, 4, v1
	v_lshlrev_b32_e32 v219, 3, v1
	v_mov_b32_e32 v223, 0x11540
	v_bfrev_b32_e32 v199, 1
	v_mov_b32_e32 v198, 1
	v_and_b32_e32 v221, 15, v1
	v_mov_b32_e32 v200, 0
	v_mov_b32_e32 v201, 0
	v_mov_b32_e32 v202, 0
	v_mov_b32_e32 v203, 0
	v_mov_b32_e32 v204, 0
	v_mov_b32_e32 v205, 0
	v_mov_b32_e32 v206, 0
	v_mov_b32_e32 v207, 0
	s_mov_b32 s50, -1
	s_waitcnt vmcnt(0)
	v_mul_f32_e32 v150, v62, v62
	v_mul_f32_e32 v151, v63, v63
	v_mul_f32_e32 v152, v64, v64
	v_mul_f32_e32 v153, v65, v65
	v_fmac_f32_e32 v150, v58, v58
	v_fmac_f32_e32 v151, v59, v59
	v_fmac_f32_e32 v152, v60, v60
	v_fmac_f32_e32 v153, v61, v61
	v_fmac_f32_e32 v150, v54, v54
	v_fmac_f32_e32 v151, v55, v55
	v_fmac_f32_e32 v152, v56, v56
	v_fmac_f32_e32 v153, v57, v57
	v_fmac_f32_e32 v150, v50, v50
	v_fmac_f32_e32 v151, v51, v51
	v_fmac_f32_e32 v152, v52, v52
	v_fmac_f32_e32 v153, v53, v53
	v_fmac_f32_e32 v150, v46, v46
	v_fmac_f32_e32 v151, v47, v47
	v_fmac_f32_e32 v152, v48, v48
	v_fmac_f32_e32 v153, v49, v49
	v_fmac_f32_e32 v150, v42, v42
	v_fmac_f32_e32 v151, v43, v43
	v_fmac_f32_e32 v152, v44, v44
	v_fmac_f32_e32 v153, v45, v45
	v_fmac_f32_e32 v150, v38, v38
	v_fmac_f32_e32 v151, v39, v39
	v_fmac_f32_e32 v152, v40, v40
	v_fmac_f32_e32 v153, v41, v41
	v_fmac_f32_e32 v150, v34, v34
	v_fmac_f32_e32 v151, v35, v35
	v_fmac_f32_e32 v152, v36, v36
	v_fmac_f32_e32 v153, v37, v37
	v_fmac_f32_e32 v150, v30, v30
	v_fmac_f32_e32 v151, v31, v31
	v_fmac_f32_e32 v152, v32, v32
	v_fmac_f32_e32 v153, v33, v33
	v_fmac_f32_e32 v150, v26, v26
	v_fmac_f32_e32 v151, v27, v27
	v_fmac_f32_e32 v152, v28, v28
	v_fmac_f32_e32 v153, v29, v29
	v_fmac_f32_e32 v150, v22, v22
	v_fmac_f32_e32 v151, v23, v23
	v_fmac_f32_e32 v152, v24, v24
	v_fmac_f32_e32 v153, v25, v25
	v_fmac_f32_e32 v150, v18, v18
	v_fmac_f32_e32 v151, v19, v19
	v_fmac_f32_e32 v152, v20, v20
	v_fmac_f32_e32 v153, v21, v21
	v_fmac_f32_e32 v150, v14, v14
	v_fmac_f32_e32 v151, v15, v15
	v_fmac_f32_e32 v152, v16, v16
	v_fmac_f32_e32 v153, v17, v17
	v_fmac_f32_e32 v150, v10, v10
	v_fmac_f32_e32 v151, v11, v11
	v_fmac_f32_e32 v152, v12, v12
	v_fmac_f32_e32 v153, v13, v13
	v_fmac_f32_e32 v150, v6, v6
	v_fmac_f32_e32 v151, v7, v7
	v_fmac_f32_e32 v152, v8, v8
	v_fmac_f32_e32 v153, v9, v9
	v_fmac_f32_e32 v150, v2, v2
	v_fmac_f32_e32 v151, v3, v3
	v_fmac_f32_e32 v152, v4, v4
	v_fmac_f32_e32 v153, v5, v5
	v_add_f32_e32 v150, v150, v151
	v_add_f32_e32 v152, v152, v153
	v_add_f32_e32 v150, v150, v152
	v_mbcnt_lo_u32_b32 v151, -1, 0
	v_mbcnt_hi_u32_b32 v151, -1, v151
	v_xor_b32_e32 v152, 16, v151
	v_lshlrev_b32_e32 v152, 2, v152
	ds_bpermute_b32 v152, v152, v150
	v_xor_b32_e32 v153, 32, v151
	v_lshlrev_b32_e32 v153, 2, v153
	s_waitcnt lgkmcnt(0)
	v_add_f32_e32 v150, v150, v152
	ds_bpermute_b32 v153, v153, v150
	v_add_u32_e32 v152, s24, v1
	v_lshlrev_b32_e32 v152, 2, v152
	v_add_u32_e32 v152, 0x11300, v152
	v_cmp_gt_u32_e32 vcc, 16, v1
	s_and_saveexec_b64 s[30:31], vcc
	s_waitcnt lgkmcnt(0)
	v_add_f32_e32 v150, v150, v153
	ds_write_b32 v152, v150
	s_mov_b64 exec, s[30:31]
	s_branch .Lg0_start
